# attention queue claim requested one unit ahead; MOE1 gather-list loads issued together; PROJ stagger
# speedup vs baseline: 1.0083x; 1.0083x over previous
.LBB0_870:
	s_mov_b32 s98, 0
	s_mov_b32 s99, 0
	s_cmp_lg_u32 0, -1
	s_cselect_b32 s2, 0, 0
	s_addk_i32 s2, 0x6000
	s_waitcnt lgkmcnt(0)
	s_add_u32 s28, s52, 0x9200
	s_addc_u32 s29, s53, 0
	s_add_u32 s30, s52, 0x9000
	s_addc_u32 s31, s53, 0
	s_add_u32 s34, s52, 0x9040
	s_addc_u32 s35, s53, 0
	s_add_u32 s36, s52, 0x9080
	s_addc_u32 s37, s53, 0
	s_add_u32 s38, s52, 0x90c0
	s_addc_u32 s39, s53, 0
	s_add_u32 s54, s52, 0x9100
	s_addc_u32 s55, s53, 0
	s_add_u32 s56, s52, 0x9140
	s_addc_u32 s57, s53, 0
	s_add_u32 s58, s52, 0x9180
	s_addc_u32 s59, s53, 0
	s_add_u32 s60, s52, 0x91c0
	v_lshlrev_b32_e32 v6, 1, v0
	s_addc_u32 s61, s53, 0
	v_and_b32_e32 v5, 63, v0
	v_and_b32_e32 v226, 31, v0
	v_and_b32_e32 v6, 32, v6
	v_lshlrev_b32_e32 v10, 4, v0
	s_add_u32 s48, s52, 0x2ac00000
	v_bfe_u32 v7, v0, 5, 1
	v_lshlrev_b32_e32 v2, 10, v5
	v_lshlrev_b32_e32 v8, 3, v0
	v_add_u32_e32 v9, s2, v6
	v_and_b32_e32 v10, 0xc0, v10
	v_add_u32_e32 v13, 0, v6
	v_lshlrev_b32_e32 v6, 10, v226
	v_cmp_gt_u32_e64 s[20:21], 32, v5
	v_bfe_u32 v5, v0, 3, 3
	s_addc_u32 s49, s53, 0
	v_and_b32_e32 v4, 24, v8
	v_lshl_or_b32 v10, v7, 8, v10
	v_lshlrev_b32_e32 v11, 10, v7
	v_lshlrev_b32_e32 v12, 4, v226
	v_lshl_or_b32 v6, v7, 3, v6
	v_lshlrev_b32_e32 v231, 4, v7
	v_lshlrev_b32_e32 v232, 9, v7
	v_or_b32_e32 v7, 8, v5
	s_add_u32 s84, s52, 0x2cc00000
	v_add3_u32 v228, 0, v11, v12
	v_add3_u32 v229, v13, v4, v10
	v_add3_u32 v230, v9, v4, v10
	v_lshlrev_b32_e32 v233, 7, v5
	v_lshlrev_b32_e32 v10, 10, v5
	v_lshlrev_b32_e32 v234, 7, v7
	v_lshlrev_b32_e32 v12, 10, v7
	v_or_b32_e32 v7, 16, v5
	v_or_b32_e32 v5, 24, v5
	s_addc_u32 s85, s53, 0
	v_and_b32_e32 v8, 56, v8
	v_lshlrev_b32_e32 v14, 10, v7
	v_lshlrev_b32_e32 v16, 10, v5
	s_add_u32 s86, s52, 0x2ec00000
	s_mov_b32 s70, 0xfffe0000
	s_mov_b32 s23, 0
	v_cmp_eq_u32_e64 s[0:1], 0, v0
	v_mov_b32_e32 v3, 0
	v_bfe_u32 v227, v0, 2, 4
	v_lshlrev_b32_e32 v235, 7, v7
	v_lshlrev_b32_e32 v236, 7, v5
	s_addc_u32 s87, s53, 0
	s_mov_b64 s[4:5], 0
	v_mov_b32_e32 v237, 0x22180
	s_mov_b32 s27, 0x20000
	s_mov_b32 s26, 0x800000
	s_movk_i32 s88, 0xff
	s_movk_i32 s89, 0x100
	s_mov_b64 s[62:63], 0x20000
	s_mov_b64 s[64:65], 0x40000
	s_mov_b64 s[66:67], 0x60000
	s_mov_b64 s[68:69], 0xa0000
	s_mov_b32 s71, -1
	s_mov_b32 s90, 0x41000000
	s_mov_b64 s[72:73], 0x80000
	s_mov_b32 s91, 0x3cc00000
	v_lshlrev_b32_e32 v206, 1, v8
	v_lshlrev_b32_e32 v208, 1, v10
	v_lshlrev_b32_e32 v210, 1, v12
	v_lshlrev_b32_e32 v212, 1, v14
	v_lshlrev_b32_e32 v214, 1, v16
	v_lshlrev_b32_e32 v216, 1, v2
	v_lshlrev_b32_e32 v218, 1, v4
	v_lshlrev_b32_e32 v238, 1, v6
	v_mov_b32_e32 v239, 0xff800000
	s_mov_b64 s[24:25], 0
	s_branch .LBB0_873

.LBB0_889:
	s_andn2_b64 vcc, exec, s[6:7]
	s_mov_b64 s[4:5], -1
	s_cbranch_vccnz .LBB0_872
	s_cmp_lg_u32 s98, 0
	s_cbranch_scc1 .Lap_use
	s_waitcnt vmcnt(0)
	s_barrier
	s_and_saveexec_b64 s[74:75], s[0:1]
	s_cbranch_execz .LBB0_904
	s_mov_b64 s[4:5], exec
	v_mbcnt_lo_u32_b32 v2, s4, 0
	s_getreg_b32 s3, hwreg(HW_REG_XCC_ID, 0, 4)
	v_mbcnt_hi_u32_b32 v2, s5, v2
	s_and_b32 s2, s3, 7
	v_cmp_eq_u32_e32 vcc, 0, v2
	s_and_saveexec_b64 s[6:7], vcc
	s_cbranch_execz .LBB0_893
	s_lshl_b32 s8, s2, 6
	s_bcnt1_i32_b64 s4, s[4:5]
	v_mov_b32_e32 v4, s8
	v_mov_b32_e32 v5, s4
	global_atomic_add v4, v4, v5, s[30:31] sc0

.Lap_join:
	v_readfirstlane_b32 s4, v4
	s_nop 1
	v_add_u32_e32 v4, s4, v2
	v_cmp_lt_u32_e32 vcc, s88, v4
	s_and_saveexec_b64 s[4:5], vcc
	s_xor_b64 s[76:77], exec, s[4:5]
	s_cbranch_execz .LBB0_901
	global_load_dword v2, v3, s[30:31] sc1
	global_load_dword v4, v3, s[34:35] sc1
	global_load_dword v5, v3, s[36:37] sc1
	global_load_dword v6, v3, s[38:39] sc1
	global_load_dword v7, v3, s[54:55] sc1
	global_load_dword v8, v3, s[56:57] sc1
	global_load_dword v9, v3, s[58:59] sc1
	global_load_dword v10, v3, s[60:61] sc1
	s_mov_b32 s22, 1
	s_mov_b64 s[78:79], 0
	s_waitcnt vmcnt(7)
	v_cmp_gt_u32_e64 s[4:5], s89, v2
	s_waitcnt vmcnt(6)
	v_cmp_gt_u32_e64 s[6:7], s89, v4
	s_waitcnt vmcnt(5)
	v_cmp_gt_u32_e64 s[8:9], s89, v5
	s_waitcnt vmcnt(4)
	v_cmp_gt_u32_e64 s[10:11], s89, v6
	s_waitcnt vmcnt(3)
	v_cmp_gt_u32_e64 s[12:13], s89, v7
	s_waitcnt vmcnt(2)
	v_cmp_gt_u32_e64 s[14:15], s89, v8
	s_waitcnt vmcnt(1)
	v_cmp_gt_u32_e64 s[16:17], s89, v9
	s_waitcnt vmcnt(0)
	v_cmp_gt_u32_e64 s[18:19], s89, v10
	s_branch .LBB0_897

.LBB0_904:
	s_or_b64 exec, exec, s[74:75]
	s_waitcnt lgkmcnt(0)
	s_barrier
	ds_read_b32 v2, v237
	s_mov_b64 s[4:5], -1
	s_waitcnt lgkmcnt(0)
	v_readfirstlane_b32 s2, v2
	s_cmp_lt_i32 s2, 0
	s_cbranch_scc1 .LBB0_872
	s_getreg_b32 s100, hwreg(HW_REG_XCC_ID, 0, 4)
	s_and_b32 s100, s100, 7
	s_lshl_b32 s100, s100, 6
	v_mov_b32_e32 v252, s100
	s_and_saveexec_b64 s[100:101], s[0:1]
	s_cbranch_execz .Lap_skip
	v_mov_b32_e32 v253, 1
	s_nop 0
	global_atomic_add v251, v252, v253, s[30:31] sc0
.Lap_skip:
	s_or_b64 exec, exec, s[100:101]
	s_mov_b32 s98, 1
	s_lshr_b32 s3, s2, 5
	s_and_b32 s3, s3, 6
	s_bfe_u32 s4, s2, 0x10002
	s_or_b32 s3, s3, s4
	s_bfe_u32 s6, s2, 0x30003
	s_xor_b32 s18, s6, 7
	s_lshr_b32 s22, s2, 8
	s_bfe_u32 s74, s2, 0x10001
	s_and_b32 s2, s2, 1
	s_lshl_b32 s3, s3, 1
	v_readfirstlane_b32 s75, v0
	s_or_b32 s7, s3, s74
	s_or_b32 s12, s3, s2
	s_lshr_b32 s19, s75, 6
	s_lshl_b64 s[2:3], s[22:23], 11
	s_lshl_b32 s10, s18, 8
	s_or_b32 s2, s2, s10
	s_lshl_b32 s11, s19, 5
	s_add_u32 s4, s2, s11
	s_addc_u32 s5, s3, 0
	s_lshl_b64 s[2:3], s[4:5], 11
	s_add_u32 s2, s48, s2
	s_addc_u32 s3, s49, s3
	s_lshl_b32 s7, s7, 7
	s_add_u32 s8, s2, s7
	s_addc_u32 s9, s3, 0
	s_lshl_b64 s[2:3], s[22:23], 22
	s_add_u32 s13, s84, s2
	s_addc_u32 s15, s85, s3
	s_add_u32 s14, s13, s7
	s_addc_u32 s15, s15, 0
	s_add_u32 s2, s86, s2
	s_addc_u32 s3, s87, s3
	s_lshl_b32 s7, s12, 7
	s_add_u32 s16, s2, s7
	v_mov_b32_e32 v217, v3
	s_addc_u32 s17, s3, 0
	v_lshl_add_u64 v[4:5], s[14:15], 0, v[216:217]
	s_lshl_b32 s22, s19, 4
	s_lshr_b32 s3, s75, 2
	s_and_b32 s2, s75, 0x3fffffc0
	v_lshl_add_u64 v[220:221], v[4:5], 0, s[22:23]
	v_and_or_b32 v2, s3, 48, v227
	s_and_b32 s22, s3, 0x3fffffc0
	s_lshl_b32 s76, s19, 10
	v_lshlrev_b32_e32 v2, 11, v2
	s_cmp_lg_u32 0, -1
	v_lshl_add_u64 v[4:5], s[16:17], 0, v[2:3]
	s_cselect_b32 s3, 0, 0
	v_lshl_add_u64 v[4:5], v[4:5], 0, s[22:23]
	v_mov_b32_e32 v219, v3
	s_add_i32 s76, s76, s3
	s_mov_b32 s3, m0
	s_mov_b32 m0, s76
	s_nop 0
	global_load_lds_dwordx4 v[220:221], off
	s_mov_b32 m0, s3
	v_lshl_add_u64 v[222:223], v[4:5], 0, v[218:219]
	s_add_i32 s77, s76, 0x6000
	s_mov_b32 s3, m0
	s_mov_b32 m0, s77
	s_nop 0
	global_load_lds_dwordx4 v[222:223], off
	s_mov_b32 m0, s3
	v_lshl_add_u64 v[4:5], v[220:221], 0, s[62:63]
	s_add_i32 s3, s76, 0x2000
	s_mov_b32 s7, m0
	s_mov_b32 m0, s3
	s_nop 0
	global_load_lds_dwordx4 v[4:5], off
	s_mov_b32 m0, s7
	global_load_dwordx4 v[158:161], v238, s[8:9]
	global_load_dwordx4 v[150:153], v238, s[8:9] offset:32
	global_load_dwordx4 v[142:145], v238, s[8:9] offset:64
	global_load_dwordx4 v[138:141], v238, s[8:9] offset:96
	v_mov_b32_e32 v16, v3
	v_mov_b32_e32 v17, v3
	v_mov_b32_e32 v4, v3
	v_mov_b32_e32 v5, v3
	v_mov_b32_e32 v6, v3
	v_mov_b32_e32 v7, v3
	v_mov_b32_e32 v8, v3
	v_mov_b32_e32 v9, v3
	v_mov_b32_e32 v10, v3
	v_mov_b32_e32 v11, v3
	v_mov_b32_e32 v12, v3
	v_mov_b32_e32 v13, v3
	v_mov_b32_e32 v14, v3
	v_mov_b32_e32 v15, v3
	v_mov_b32_e32 v2, v3
	v_mov_b64_e32 v[32:33], v[16:17]
	v_mov_b64_e32 v[30:31], v[14:15]
	v_mov_b64_e32 v[28:29], v[12:13]
	v_mov_b64_e32 v[26:27], v[10:11]
	v_mov_b64_e32 v[24:25], v[8:9]
	v_mov_b64_e32 v[22:23], v[6:7]
	v_mov_b64_e32 v[20:21], v[4:5]
	v_mov_b64_e32 v[18:19], v[2:3]
	v_lshl_add_u64 v[34:35], v[220:221], 0, s[64:65]
	s_add_i32 s3, s76, 0x4000
	s_mov_b32 s7, m0
	s_mov_b32 m0, s3
	s_nop 0
	global_load_lds_dwordx4 v[34:35], off
	s_mov_b32 m0, s7
	s_waitcnt vmcnt(3) lgkmcnt(0)
	s_barrier
	ds_read_b128 v[50:53], v228
	ds_read_b128 v[54:57], v228 offset:512
	s_add_i32 s7, s10, 0x100
	s_lshl_b32 s2, s2, 2
	s_add_i32 s22, s2, 0
	s_lshr_b32 s2, s7, 6
	s_mov_b32 s8, 1
	s_mov_b32 s13, 0
	s_movk_i32 s3, 0x2000
	s_movk_i32 s40, 0x4000
	v_lshl_add_u32 v207, v226, 2, s22
	s_waitcnt vmcnt(3) lgkmcnt(1)
	v_mfma_f32_32x32x16_bf16 v[34:49], v[50:53], v[158:161], v[18:33]
	s_waitcnt lgkmcnt(0)
	v_mfma_f32_32x32x16_bf16 v[18:33], v[54:57], v[158:161], v[18:33]
	ds_read_b128 v[50:53], v228 offset:2048
	ds_read_b128 v[54:57], v228 offset:2560
	s_waitcnt vmcnt(2) lgkmcnt(1)
	v_mfma_f32_32x32x16_bf16 v[34:49], v[50:53], v[150:153], v[34:49]
	s_waitcnt lgkmcnt(0)
	v_mfma_f32_32x32x16_bf16 v[18:33], v[54:57], v[150:153], v[18:33]
	ds_read_b128 v[50:53], v228 offset:4096
	ds_read_b128 v[54:57], v228 offset:4608
	s_waitcnt vmcnt(1) lgkmcnt(1)
	v_mfma_f32_32x32x16_bf16 v[34:49], v[50:53], v[142:145], v[34:49]
	s_waitcnt lgkmcnt(0)
	v_mfma_f32_32x32x16_bf16 v[18:33], v[54:57], v[142:145], v[18:33]
	ds_read_b128 v[50:53], v228 offset:6144
	ds_read_b128 v[54:57], v228 offset:6656
	s_waitcnt vmcnt(0) lgkmcnt(1)
	v_mfma_f32_32x32x16_bf16 v[34:49], v[50:53], v[138:141], v[34:49]
	s_waitcnt lgkmcnt(0)
	v_mfma_f32_32x32x16_bf16 v[18:33], v[54:57], v[138:141], v[18:33]
	s_nop 15
	s_nop 7
	s_nop 0
	v_max3_f32 v50, v34, v35, v18
	v_max3_f32 v51, v36, v37, v19
	s_nop 0
	v_max3_f32 v50, v50, v20, v21
	v_max3_f32 v51, v51, v40, v41
	s_nop 0
	v_max3_f32 v50, v50, v38, v39
	v_max3_f32 v51, v51, v24, v25
	s_nop 0
	v_max3_f32 v50, v50, v22, v23
	v_max3_f32 v51, v51, v44, v45
	s_nop 0
	v_max3_f32 v50, v50, v42, v43
	v_max3_f32 v51, v51, v28, v29
	s_nop 0
	v_max3_f32 v50, v50, v26, v27
	v_max3_f32 v51, v51, v48, v49
	s_nop 0
	v_max3_f32 v50, v50, v46, v47
	v_max3_f32 v51, v51, v32, v33
	s_nop 0
	v_max3_f32 v50, v50, v30, v31
	s_nop 0
	v_max_f32_e32 v50, v50, v51
	s_nop 0
	v_mov_b32_e32 v51, v50
	s_nop 1
	v_permlane32_swap_b32_e32 v50, v51
	v_max_f32_e32 v50, v50, v51
	s_nop 0
	v_add_f32_e32 v209, v3, v50
	v_sub_f32_e32 v34, v34, v50
	v_sub_f32_e32 v18, v18, v50
	v_sub_f32_e32 v35, v35, v50
	v_sub_f32_e32 v19, v19, v50
	v_sub_f32_e32 v36, v36, v50
	v_sub_f32_e32 v20, v20, v50
	v_sub_f32_e32 v37, v37, v50
	v_sub_f32_e32 v21, v21, v50
	v_sub_f32_e32 v38, v38, v50
	v_sub_f32_e32 v22, v22, v50
	v_sub_f32_e32 v39, v39, v50
	v_sub_f32_e32 v23, v23, v50
	v_sub_f32_e32 v40, v40, v50
	v_sub_f32_e32 v24, v24, v50
	v_sub_f32_e32 v41, v41, v50
	v_sub_f32_e32 v25, v25, v50
	v_sub_f32_e32 v42, v42, v50
	v_sub_f32_e32 v26, v26, v50
	v_sub_f32_e32 v43, v43, v50
	v_sub_f32_e32 v27, v27, v50
	v_sub_f32_e32 v44, v44, v50
	v_sub_f32_e32 v28, v28, v50
	v_sub_f32_e32 v45, v45, v50
	v_sub_f32_e32 v29, v29, v50
	v_sub_f32_e32 v46, v46, v50
	v_sub_f32_e32 v30, v30, v50
	v_sub_f32_e32 v47, v47, v50
	v_sub_f32_e32 v31, v31, v50
	v_sub_f32_e32 v48, v48, v50
	v_sub_f32_e32 v32, v32, v50
	v_sub_f32_e32 v49, v49, v50
	v_sub_f32_e32 v33, v33, v50
	s_nop 0
	v_xor_b32_e32 v50, 0x80000000, v209
	v_mov_b32_e32 v51, v50
	v_mov_b32_e32 v52, v50
	v_mov_b32_e32 v53, v50
	v_mov_b32_e32 v54, v50
	v_mov_b32_e32 v55, v50
	v_mov_b32_e32 v56, v50
	v_mov_b32_e32 v57, v50
	v_mov_b32_e32 v58, v50
	v_mov_b32_e32 v59, v50
	v_mov_b32_e32 v60, v50
	v_mov_b32_e32 v61, v50
	v_mov_b32_e32 v62, v50
	v_mov_b32_e32 v63, v50
	v_mov_b32_e32 v64, v50
	v_mov_b32_e32 v65, v50
	s_waitcnt vmcnt(0) lgkmcnt(0)
	s_barrier
	v_exp_f32_e32 v66, v18
	v_exp_f32_e32 v67, v19
	v_lshl_add_u64 v[18:19], v[220:221], 0, s[66:67]
	s_mov_b32 s7, m0
	s_mov_b32 m0, s76
	s_nop 0
	global_load_lds_dwordx4 v[18:19], off
	s_mov_b32 m0, s7
	v_lshl_add_u64 v[18:19], v[222:223], 0, s[62:63]
	s_add_i32 s7, s76, 0x8000
	s_mov_b32 s9, m0
	s_mov_b32 m0, s7
	s_nop 0
	global_load_lds_dwordx4 v[18:19], off
	s_mov_b32 m0, s9
	ds_read_b128 v[190:193], v228 offset:8192
	ds_read_b128 v[186:189], v228 offset:8704
	ds_read_b128 v[182:185], v228 offset:10240
	ds_read_b128 v[178:181], v228 offset:10752
	ds_read_b128 v[174:177], v228 offset:12288
	ds_read_b128 v[170:173], v228 offset:12800
	ds_read_b128 v[166:169], v228 offset:14336
	ds_read_b128 v[162:165], v228 offset:14848
	v_exp_f32_e32 v82, v34
	v_exp_f32_e32 v83, v35
	v_exp_f32_e32 v84, v36
	v_exp_f32_e32 v85, v37
	v_exp_f32_e32 v86, v38
	v_exp_f32_e32 v87, v39
	v_exp_f32_e32 v88, v40
	v_exp_f32_e32 v89, v41
	v_exp_f32_e32 v90, v42
	v_exp_f32_e32 v91, v43
	v_exp_f32_e32 v92, v44
	v_exp_f32_e32 v93, v45
	v_exp_f32_e32 v94, v46
	v_exp_f32_e32 v95, v47
	v_exp_f32_e32 v96, v48
	v_exp_f32_e32 v97, v49
	v_exp_f32_e32 v68, v20
	v_exp_f32_e32 v69, v21
	v_exp_f32_e32 v70, v22
	v_exp_f32_e32 v71, v23
	v_exp_f32_e32 v72, v24
	v_exp_f32_e32 v73, v25
	v_exp_f32_e32 v74, v26
	v_exp_f32_e32 v75, v27
	v_exp_f32_e32 v76, v28
	v_exp_f32_e32 v77, v29
	v_exp_f32_e32 v78, v30
	v_exp_f32_e32 v79, v31
	v_exp_f32_e32 v80, v32
	v_exp_f32_e32 v81, v33
	s_waitcnt vmcnt(2) lgkmcnt(0)
	s_barrier
	s_cmp_eq_u32 s6, 7
	s_cbranch_scc1 .LBB0_921
	v_mov_b32_e32 v16, v3
	v_mov_b32_e32 v17, v3
	v_mov_b32_e32 v2, v3
	v_mov_b32_e32 v4, v3
	v_mov_b32_e32 v5, v3
	v_mov_b32_e32 v6, v3
	v_mov_b32_e32 v7, v3
	v_mov_b32_e32 v8, v3
	v_mov_b32_e32 v9, v3
	v_mov_b32_e32 v10, v3
	v_mov_b32_e32 v11, v3
	v_mov_b32_e32 v12, v3
	v_mov_b32_e32 v13, v3
	v_mov_b32_e32 v14, v3
	v_mov_b32_e32 v15, v3
	v_mov_b64_e32 v[48:49], v[16:17]
	v_mov_b64_e32 v[32:33], v[16:17]
	v_lshl_add_u64 v[198:199], v[222:223], 0, s[66:67]
	v_lshl_add_u64 v[200:201], v[220:221], 0, s[68:69]
	s_mov_b32 s6, 0
	s_movk_i32 s13, 0x4000
	s_movk_i32 s15, 0x2000
	v_mov_b32_e32 v211, 0
	s_mov_b32 s14, 6
	v_mov_b64_e32 v[46:47], v[14:15]
	v_mov_b64_e32 v[44:45], v[12:13]
	v_mov_b64_e32 v[42:43], v[10:11]
	v_mov_b64_e32 v[40:41], v[8:9]
	v_mov_b64_e32 v[38:39], v[6:7]
	v_mov_b64_e32 v[36:37], v[4:5]
	v_mov_b64_e32 v[34:35], v[2:3]
	v_mov_b64_e32 v[30:31], v[14:15]
	v_mov_b64_e32 v[28:29], v[12:13]
	v_mov_b64_e32 v[26:27], v[10:11]
	v_mov_b64_e32 v[24:25], v[8:9]
	v_mov_b64_e32 v[22:23], v[6:7]
	v_mov_b64_e32 v[20:21], v[4:5]
	v_mov_b64_e32 v[18:19], v[2:3]

.Lap_use:
	s_mov_b32 s98, 0
	s_barrier
	s_and_saveexec_b64 s[74:75], s[0:1]
	s_cbranch_execz .LBB0_904
	s_mov_b64 s[4:5], exec
	v_mbcnt_lo_u32_b32 v2, s4, 0
	s_getreg_b32 s3, hwreg(HW_REG_XCC_ID, 0, 4)
	v_mbcnt_hi_u32_b32 v2, s5, v2
	s_and_b32 s2, s3, 7
	s_waitcnt vmcnt(8)
	v_mov_b32_e32 v4, v251
	s_nop 1
	s_branch .Lap_join

.LBB0_1353:
	s_nop 0
	v_cndmask_b32_e64 v2, 0, 1, s[4:5]
	v_cmp_ne_u32_e64 s[0:1], 1, v2
	s_andn2_b64 vcc, exec, s[4:5]
	v_mov_b64_e32 v[214:215], v[206:207]
	v_mov_b32_e32 v212, v204
	v_mov_b32_e32 v210, v194
	v_mov_b32_e32 v243, v198
	v_mov_b32_e32 v244, v196
	s_cbranch_vccnz .LBB0_1363
	v_lshlrev_b32_e32 v2, 14, v208
	v_lshlrev_b32_e32 v3, 8, v242
	v_add_u32_e32 v4, v3, v2
	v_mov_b32_e32 v3, 0
	v_mov_b32_e32 v2, 0
	v_mov_b32_e32 v6, 0
	v_mov_b32_e32 v5, 0
	v_cmp_lt_i32_e32 vcc, v220, v241
	s_and_saveexec_b64 s[4:5], vcc
	s_cbranch_execz .Lm1s_0
	v_add_u32_e32 v8, v4, v220
	v_ashrrev_i32_e32 v9, 31, v8
	v_lshl_add_u64 v[8:9], v[8:9], 2, s[10:11]
	global_load_dword v2, v[8:9], off
.Lm1s_0:
	s_or_b64 exec, exec, s[4:5]
	v_cmp_lt_i32_e32 vcc, v221, v241
	s_and_saveexec_b64 s[4:5], vcc
	s_cbranch_execz .Lm1s_1
	v_add_u32_e32 v10, v4, v221
	v_ashrrev_i32_e32 v11, 31, v10
	v_lshl_add_u64 v[10:11], v[10:11], 2, s[10:11]
	global_load_dword v3, v[10:11], off
.Lm1s_1:
	s_or_b64 exec, exec, s[4:5]
	v_cmp_lt_i32_e32 vcc, v245, v241
	s_and_saveexec_b64 s[4:5], vcc
	s_cbranch_execz .Lm1s_2
	v_add_u32_e32 v12, v4, v245
	v_ashrrev_i32_e32 v13, 31, v12
	v_lshl_add_u64 v[12:13], v[12:13], 2, s[10:11]
	global_load_dword v6, v[12:13], off
.Lm1s_2:
	s_or_b64 exec, exec, s[4:5]
	v_cmp_lt_i32_e32 vcc, v254, v241
	s_and_saveexec_b64 s[4:5], vcc
	s_cbranch_execz .Lm1s_3
	v_add_u32_e32 v14, v4, v254
	v_ashrrev_i32_e32 v15, 31, v14
	v_lshl_add_u64 v[14:15], v[14:15], 2, s[10:11]
	global_load_dword v5, v[14:15], off
.Lm1s_3:
	s_or_b64 exec, exec, s[4:5]
	s_waitcnt vmcnt(0)
	v_lshlrev_b32_e32 v2, 11, v2
	v_lshlrev_b32_e32 v3, 11, v3
	v_lshlrev_b32_e32 v6, 11, v6
	v_lshlrev_b32_e32 v5, 11, v5

	.amdhsa_kernel _Z6mk_fwd4Args
		.amdhsa_group_segment_fixed_size 0
		.amdhsa_private_segment_fixed_size 0
		.amdhsa_kernarg_size 488
		.amdhsa_user_sgpr_count 2
		.amdhsa_user_sgpr_dispatch_ptr 0
		.amdhsa_user_sgpr_queue_ptr 0
		.amdhsa_user_sgpr_kernarg_segment_ptr 1
		.amdhsa_user_sgpr_dispatch_id 0
		.amdhsa_user_sgpr_kernarg_preload_length 0
		.amdhsa_user_sgpr_kernarg_preload_offset 0
		.amdhsa_user_sgpr_private_segment_size 0
		.amdhsa_uses_dynamic_stack 0
		.amdhsa_enable_private_segment 0
		.amdhsa_system_sgpr_workgroup_id_x 1
		.amdhsa_system_sgpr_workgroup_id_y 0
		.amdhsa_system_sgpr_workgroup_id_z 0
		.amdhsa_system_sgpr_workgroup_info 0
		.amdhsa_system_vgpr_workitem_id 0
		.amdhsa_next_free_vgpr 256
		.amdhsa_next_free_sgpr 102
		.amdhsa_accum_offset 256
		.amdhsa_reserve_vcc 1
		.amdhsa_float_round_mode_32 0
		.amdhsa_float_round_mode_16_64 0
		.amdhsa_float_denorm_mode_32 3
		.amdhsa_float_denorm_mode_16_64 3
		.amdhsa_dx10_clamp 1
		.amdhsa_ieee_mode 1
		.amdhsa_fp16_overflow 0
		.amdhsa_tg_split 0
		.amdhsa_exception_fp_ieee_invalid_op 0
		.amdhsa_exception_fp_denorm_src 0
		.amdhsa_exception_fp_ieee_div_zero 0
		.amdhsa_exception_fp_ieee_overflow 0
		.amdhsa_exception_fp_ieee_underflow 0
		.amdhsa_exception_fp_ieee_inexact 0
		.amdhsa_exception_int_div_zero 0
	.end_amdhsa_kernel

.Lfunc_end0:
	.size	_Z6mk_fwd4Args, .Lfunc_end0-_Z6mk_fwd4Args
	.set _Z6mk_fwd4Args.num_vgpr, 256
	.set _Z6mk_fwd4Args.num_agpr, 0
	.set _Z6mk_fwd4Args.numbered_sgpr, 102
	.set _Z6mk_fwd4Args.num_named_barrier, 0
	.set _Z6mk_fwd4Args.private_seg_size, 0
	.set _Z6mk_fwd4Args.uses_vcc, 1
	.set _Z6mk_fwd4Args.uses_flat_scratch, 0
	.set _Z6mk_fwd4Args.has_dyn_sized_stack, 0
	.set _Z6mk_fwd4Args.has_recursion, 0
	.set _Z6mk_fwd4Args.has_indirect_call, 0

amdhsa.kernels:
  - .agpr_count:     0
    .args:
      - .offset:         0
        .size:           232
        .value_kind:     by_value
      - .offset:         232
        .size:           4
        .value_kind:     hidden_block_count_x
      - .offset:         236
        .size:           4
        .value_kind:     hidden_block_count_y
      - .offset:         240
        .size:           4
        .value_kind:     hidden_block_count_z
      - .offset:         244
        .size:           2
        .value_kind:     hidden_group_size_x
      - .offset:         246
        .size:           2
        .value_kind:     hidden_group_size_y
      - .offset:         248
        .size:           2
        .value_kind:     hidden_group_size_z
      - .offset:         250
        .size:           2
        .value_kind:     hidden_remainder_x
      - .offset:         252
        .size:           2
        .value_kind:     hidden_remainder_y
      - .offset:         254
        .size:           2
        .value_kind:     hidden_remainder_z
      - .offset:         272
        .size:           8
        .value_kind:     hidden_global_offset_x
      - .offset:         280
        .size:           8
        .value_kind:     hidden_global_offset_y
      - .offset:         288
        .size:           8
        .value_kind:     hidden_global_offset_z
      - .offset:         296
        .size:           2
        .value_kind:     hidden_grid_dims
      - .offset:         352
        .size:           4
        .value_kind:     hidden_dynamic_lds_size
    .group_segment_fixed_size: 0
    .kernarg_segment_align: 8
    .kernarg_segment_size: 488
    .language:       OpenCL C
    .language_version:
      - 2
      - 0
    .max_flat_workgroup_size: 512
    .name:           _Z6mk_fwd4Args
    .private_segment_fixed_size: 0
    .sgpr_count:     108
    .sgpr_spill_count: 21
    .symbol:         _Z6mk_fwd4Args.kd
    .uniform_work_group_size: 1
    .uses_dynamic_stack: false
    .vgpr_count:     256
    .vgpr_spill_count: 0
    .wavefront_size: 64
